# speedup vs baseline: 1.1641x; 1.0082x over previous
.LBB1_31:
	s_or_b64 exec, exec, s[18:19]
	s_waitcnt lgkmcnt(0)
	s_barrier
	s_mov_b32 s40, 0xc350
	s_movk_i32 s41, 0xc40
	s_waitcnt vmcnt(0)
	v_lshlrev_b32_e32 v48, 3, v0
	v_and_b32_e32 v48, 0x78, v48
	v_mov_b32_e32 v49, 0
	v_lshl_add_u64 v[48:49], s[34:35], 0, v[48:49]
	v_lshlrev_b32_e32 v50, 2, v25
	v_cmp_gt_i32_e64 s[44:45], s40, v28
	s_and_saveexec_b64 s[42:43], s[44:45]
	ds_read_b32 v51, v50 offset:19456
	v_mov_b32_e32 v52, v28
	v_mov_b32_e32 v53, 0
	v_lshlrev_b64 v[52:53], 7, v[52:53]
	s_waitcnt lgkmcnt(0)
	v_mul_f32_e32 v14, v51, v14
	v_mul_f32_e32 v15, v51, v15
	v_mul_f32_e32 v16, v51, v16
	v_mul_f32_e32 v17, v51, v17
	v_cvt_pk_f16_f32 v14, v14, v15
	v_cvt_pk_f16_f32 v15, v16, v17
	v_lshl_add_u64 v[52:53], v[48:49], 0, v[52:53]
	global_store_dwordx2 v[52:53], v[14:15], off sc0 sc1
	s_or_b64 exec, exec, s[42:43]
	v_cmp_gt_i32_e64 s[44:45], s40, v26
	s_and_saveexec_b64 s[42:43], s[44:45]
	ds_read_b32 v51, v50 offset:19712
	v_mov_b32_e32 v52, v26
	v_mov_b32_e32 v53, 0
	v_lshlrev_b64 v[52:53], 7, v[52:53]
	s_waitcnt lgkmcnt(0)
	v_mul_f32_e32 v10, v51, v10
	v_mul_f32_e32 v11, v51, v11
	v_mul_f32_e32 v12, v51, v12
	v_mul_f32_e32 v13, v51, v13
	v_cvt_pk_f16_f32 v10, v10, v11
	v_cvt_pk_f16_f32 v11, v12, v13
	v_lshl_add_u64 v[52:53], v[48:49], 0, v[52:53]
	global_store_dwordx2 v[52:53], v[10:11], off sc0 sc1
	s_or_b64 exec, exec, s[42:43]
	v_cmp_gt_i32_e64 s[44:45], s40, v24
	s_and_saveexec_b64 s[42:43], s[44:45]
	ds_read_b32 v51, v50 offset:19968
	v_mov_b32_e32 v52, v24
	v_mov_b32_e32 v53, 0
	v_lshlrev_b64 v[52:53], 7, v[52:53]
	s_waitcnt lgkmcnt(0)
	v_mul_f32_e32 v6, v51, v6
	v_mul_f32_e32 v7, v51, v7
	v_mul_f32_e32 v8, v51, v8
	v_mul_f32_e32 v9, v51, v9
	v_cvt_pk_f16_f32 v6, v6, v7
	v_cvt_pk_f16_f32 v7, v8, v9
	v_lshl_add_u64 v[52:53], v[48:49], 0, v[52:53]
	global_store_dwordx2 v[52:53], v[6:7], off sc0 sc1
	s_or_b64 exec, exec, s[42:43]
	v_cmp_gt_u32_e64 s[44:45], s41, v32
	v_cmp_gt_i32_e64 s[46:47], s40, v22
	s_and_b64 s[44:45], s[44:45], s[46:47]
	v_lshlrev_b32_e32 v54, 2, v23
	s_and_saveexec_b64 s[42:43], s[44:45]
	ds_read_b32 v51, v54 offset:19456
	v_mov_b32_e32 v52, v22
	v_mov_b32_e32 v53, 0
	v_lshlrev_b64 v[52:53], 7, v[52:53]
	s_waitcnt lgkmcnt(0)
	v_mul_f32_e32 v2, v51, v2
	v_mul_f32_e32 v3, v51, v3
	v_mul_f32_e32 v4, v51, v4
	v_mul_f32_e32 v5, v51, v5
	v_cvt_pk_f16_f32 v2, v2, v3
	v_cvt_pk_f16_f32 v3, v4, v5
	v_lshl_add_u64 v[52:53], v[48:49], 0, v[52:53]
	global_store_dwordx2 v[52:53], v[2:3], off sc0 sc1
	s_or_b64 exec, exec, s[42:43]
	s_and_saveexec_b64 s[30:31], s[8:9]
	s_cbranch_execz .LBB1_38
	v_lshrrev_b32_e32 v18, 6, v0
	v_cmp_gt_u32_e64 s[8:9], 49, v38
	v_mov_b32_e32 v19, -1
	s_and_saveexec_b64 s[12:13], s[8:9]
	s_cbranch_execz .LBB1_34
	v_mad_u32_u24 v19, v18, 49, v38
	v_lshlrev_b32_e32 v39, 2, v19
	ds_read_b32 v39, v39 offset:16384
	s_waitcnt lgkmcnt(0)
	v_lshl_or_b32 v19, v39, 8, v19

.LBB1_71:
	s_or_b64 exec, exec, s[0:1]
	s_endpgm

	.amdhsa_kernel _Z5k_csrPKjS0_PKfPjPfPDF16_P15HIP_vector_typeIjLj4EE
		.amdhsa_group_segment_fixed_size 22536
		.amdhsa_private_segment_fixed_size 0
		.amdhsa_kernarg_size 56
		.amdhsa_user_sgpr_count 2
		.amdhsa_user_sgpr_dispatch_ptr 0
		.amdhsa_user_sgpr_queue_ptr 0
		.amdhsa_user_sgpr_kernarg_segment_ptr 1
		.amdhsa_user_sgpr_dispatch_id 0
		.amdhsa_user_sgpr_kernarg_preload_length 0
		.amdhsa_user_sgpr_kernarg_preload_offset 0
		.amdhsa_user_sgpr_private_segment_size 0
		.amdhsa_uses_dynamic_stack 0
		.amdhsa_enable_private_segment 0
		.amdhsa_system_sgpr_workgroup_id_x 1
		.amdhsa_system_sgpr_workgroup_id_y 0
		.amdhsa_system_sgpr_workgroup_id_z 0
		.amdhsa_system_sgpr_workgroup_info 0
		.amdhsa_system_vgpr_workitem_id 0
		.amdhsa_next_free_vgpr 56
		.amdhsa_next_free_sgpr 48
		.amdhsa_accum_offset 56
		.amdhsa_reserve_vcc 1
		.amdhsa_float_round_mode_32 0
		.amdhsa_float_round_mode_16_64 0
		.amdhsa_float_denorm_mode_32 3
		.amdhsa_float_denorm_mode_16_64 3
		.amdhsa_dx10_clamp 1
		.amdhsa_ieee_mode 1
		.amdhsa_fp16_overflow 0
		.amdhsa_tg_split 0
		.amdhsa_exception_fp_ieee_invalid_op 0
		.amdhsa_exception_fp_denorm_src 0
		.amdhsa_exception_fp_ieee_div_zero 0
		.amdhsa_exception_fp_ieee_overflow 0
		.amdhsa_exception_fp_ieee_underflow 0
		.amdhsa_exception_fp_ieee_inexact 0
		.amdhsa_exception_int_div_zero 0
	.end_amdhsa_kernel

amdhsa.kernels:
  - .agpr_count:     0
    .args:
      - .actual_access:  read_only
        .address_space:  global
        .offset:         0
        .size:           8
        .value_kind:     global_buffer
      - .actual_access:  read_only
        .address_space:  global
        .offset:         8
        .size:           8
        .value_kind:     global_buffer
      - .actual_access:  write_only
        .address_space:  global
        .offset:         16
        .size:           8
        .value_kind:     global_buffer
      - .actual_access:  write_only
        .address_space:  global
        .offset:         24
        .size:           8
        .value_kind:     global_buffer
      - .actual_access:  read_only
        .address_space:  global
        .offset:         32
        .size:           8
        .value_kind:     global_buffer
      - .actual_access:  read_only
        .address_space:  global
        .offset:         40
        .size:           8
        .value_kind:     global_buffer
      - .actual_access:  read_only
        .address_space:  global
        .offset:         48
        .size:           8
        .value_kind:     global_buffer
      - .actual_access:  read_only
        .address_space:  global
        .offset:         56
        .size:           8
        .value_kind:     global_buffer
      - .actual_access:  read_only
        .address_space:  global
        .offset:         64
        .size:           8
        .value_kind:     global_buffer
      - .actual_access:  write_only
        .address_space:  global
        .offset:         72
        .size:           8
        .value_kind:     global_buffer
      - .actual_access:  write_only
        .address_space:  global
        .offset:         80
        .size:           8
        .value_kind:     global_buffer
      - .actual_access:  write_only
        .address_space:  global
        .offset:         88
        .size:           8
        .value_kind:     global_buffer
      - .actual_access:  write_only
        .address_space:  global
        .offset:         96
        .size:           8
        .value_kind:     global_buffer
      - .actual_access:  write_only
        .address_space:  global
        .offset:         104
        .size:           8
        .value_kind:     global_buffer
      - .actual_access:  write_only
        .address_space:  global
        .offset:         112
        .size:           8
        .value_kind:     global_buffer
      - .offset:         120
        .size:           4
        .value_kind:     hidden_block_count_x
      - .offset:         124
        .size:           4
        .value_kind:     hidden_block_count_y
      - .offset:         128
        .size:           4
        .value_kind:     hidden_block_count_z
      - .offset:         132
        .size:           2
        .value_kind:     hidden_group_size_x
      - .offset:         134
        .size:           2
        .value_kind:     hidden_group_size_y
      - .offset:         136
        .size:           2
        .value_kind:     hidden_group_size_z
      - .offset:         138
        .size:           2
        .value_kind:     hidden_remainder_x
      - .offset:         140
        .size:           2
        .value_kind:     hidden_remainder_y
      - .offset:         142
        .size:           2
        .value_kind:     hidden_remainder_z
      - .offset:         160
        .size:           8
        .value_kind:     hidden_global_offset_x
      - .offset:         168
        .size:           8
        .value_kind:     hidden_global_offset_y
      - .offset:         176
        .size:           8
        .value_kind:     hidden_global_offset_z
      - .offset:         184
        .size:           2
        .value_kind:     hidden_grid_dims
    .group_segment_fixed_size: 21520
    .kernarg_segment_align: 8
    .kernarg_segment_size: 376
    .language:       OpenCL C
    .language_version:
      - 2
      - 0
    .max_flat_workgroup_size: 1024
    .name:           _Z11k_chunksortPKiS0_PjS1_PKfS3_S3_S3_S3_PDF16_S4_PfS5_S4_Ph
    .private_segment_fixed_size: 0
    .sgpr_count:     32
    .sgpr_spill_count: 0
    .symbol:         _Z11k_chunksortPKiS0_PjS1_PKfS3_S3_S3_S3_PDF16_S4_PfS5_S4_Ph.kd
    .uniform_work_group_size: 1
    .uses_dynamic_stack: false
    .vgpr_count:     38
    .vgpr_spill_count: 0
    .wavefront_size: 64
  - .agpr_count:     0
    .args:
      - .actual_access:  read_only
        .address_space:  global
        .offset:         0
        .size:           8
        .value_kind:     global_buffer
      - .actual_access:  read_only
        .address_space:  global
        .offset:         8
        .size:           8
        .value_kind:     global_buffer
      - .actual_access:  read_only
        .address_space:  global
        .offset:         16
        .size:           8
        .value_kind:     global_buffer
      - .actual_access:  write_only
        .address_space:  global
        .offset:         24
        .size:           8
        .value_kind:     global_buffer
      - .actual_access:  write_only
        .address_space:  global
        .offset:         32
        .size:           8
        .value_kind:     global_buffer
      - .actual_access:  write_only
        .address_space:  global
        .offset:         40
        .size:           8
        .value_kind:     global_buffer
      - .actual_access:  write_only
        .address_space:  global
        .offset:         48
        .size:           8
        .value_kind:     global_buffer
    .group_segment_fixed_size: 22536
    .kernarg_segment_align: 8
    .kernarg_segment_size: 56
    .language:       OpenCL C
    .language_version:
      - 2
      - 0
    .max_flat_workgroup_size: 1024
    .name:           _Z5k_csrPKjS0_PKfPjPfPDF16_P15HIP_vector_typeIjLj4EE
    .private_segment_fixed_size: 0
    .sgpr_count:     54
    .sgpr_spill_count: 0
    .symbol:         _Z5k_csrPKjS0_PKfPjPfPDF16_P15HIP_vector_typeIjLj4EE.kd
    .uniform_work_group_size: 1
    .uses_dynamic_stack: false
    .vgpr_count:     56
    .vgpr_spill_count: 0
    .wavefront_size: 64
  - .agpr_count:     0
    .args:
      - .actual_access:  read_only
        .address_space:  global
        .offset:         0
        .size:           8
        .value_kind:     global_buffer
      - .actual_access:  read_only
        .address_space:  global
        .offset:         8
        .size:           8
        .value_kind:     global_buffer
      - .actual_access:  read_only
        .address_space:  global
        .offset:         16
        .size:           8
        .value_kind:     global_buffer
      - .actual_access:  read_only
        .address_space:  global
        .offset:         24
        .size:           8
        .value_kind:     global_buffer
      - .actual_access:  read_only
        .address_space:  global
        .offset:         32
        .size:           8
        .value_kind:     global_buffer
      - .actual_access:  read_only
        .address_space:  global
        .offset:         40
        .size:           8
        .value_kind:     global_buffer
      - .actual_access:  read_only
        .address_space:  global
        .offset:         48
        .size:           8
        .value_kind:     global_buffer
      - .actual_access:  write_only
        .address_space:  global
        .offset:         56
        .size:           8
        .value_kind:     global_buffer
      - .actual_access:  write_only
        .address_space:  global
        .offset:         64
        .size:           8
        .value_kind:     global_buffer
    .group_segment_fixed_size: 36112
    .kernarg_segment_align: 8
    .kernarg_segment_size: 72
    .language:       OpenCL C
    .language_version:
      - 2
      - 0
    .max_flat_workgroup_size: 256
    .name:           _Z8k_layer1PKfPKDF16_PK15HIP_vector_typeIjLj4EEPKjS0_S2_S0_PhPf
    .private_segment_fixed_size: 0
    .sgpr_count:     30
    .sgpr_spill_count: 0
    .symbol:         _Z8k_layer1PKfPKDF16_PK15HIP_vector_typeIjLj4EEPKjS0_S2_S0_PhPf.kd
    .uniform_work_group_size: 1
    .uses_dynamic_stack: false
    .vgpr_count:     128
    .vgpr_spill_count: 0
    .wavefront_size: 64
  - .agpr_count:     0
    .args:
      - .actual_access:  read_only
        .address_space:  global
        .offset:         0
        .size:           8
        .value_kind:     global_buffer
      - .actual_access:  read_only
        .address_space:  global
        .offset:         8
        .size:           8
        .value_kind:     global_buffer
      - .actual_access:  read_only
        .address_space:  global
        .offset:         16
        .size:           8
        .value_kind:     global_buffer
      - .actual_access:  read_only
        .address_space:  global
        .offset:         24
        .size:           8
        .value_kind:     global_buffer
      - .actual_access:  read_only
        .address_space:  global
        .offset:         32
        .size:           8
        .value_kind:     global_buffer
      - .actual_access:  read_only
        .address_space:  global
        .offset:         40
        .size:           8
        .value_kind:     global_buffer
      - .actual_access:  read_only
        .address_space:  global
        .offset:         48
        .size:           8
        .value_kind:     global_buffer
      - .address_space:  global
        .offset:         56
        .size:           8
        .value_kind:     global_buffer
    .group_segment_fixed_size: 39168
    .kernarg_segment_align: 8
    .kernarg_segment_size: 64
    .language:       OpenCL C
    .language_version:
      - 2
      - 0
    .max_flat_workgroup_size: 256
    .name:           _Z8k_layer2PKhPKfPK15HIP_vector_typeIjLj4EEPKjS2_PKDF16_S2_Pf
    .private_segment_fixed_size: 0
    .sgpr_count:     27
    .sgpr_spill_count: 0
    .symbol:         _Z8k_layer2PKhPKfPK15HIP_vector_typeIjLj4EEPKjS2_PKDF16_S2_Pf.kd
    .uniform_work_group_size: 1
    .uses_dynamic_stack: false
    .vgpr_count:     128
    .vgpr_spill_count: 0
    .wavefront_size: 64
  - .agpr_count:     0
    .args:
      - .actual_access:  read_only
        .address_space:  global
        .offset:         0
        .size:           8
        .value_kind:     global_buffer
      - .actual_access:  read_only
        .address_space:  global
        .offset:         8
        .size:           8
        .value_kind:     global_buffer
      - .actual_access:  read_only
        .address_space:  global
        .offset:         16
        .size:           8
        .value_kind:     global_buffer
      - .actual_access:  read_only
        .address_space:  global
        .offset:         24
        .size:           8
        .value_kind:     global_buffer
      - .actual_access:  read_only
        .address_space:  global
        .offset:         32
        .size:           8
        .value_kind:     global_buffer
      - .actual_access:  write_only
        .address_space:  global
        .offset:         40
        .size:           8
        .value_kind:     global_buffer
    .group_segment_fixed_size: 512
    .kernarg_segment_align: 8
    .kernarg_segment_size: 48
    .language:       OpenCL C
    .language_version:
      - 2
      - 0
    .max_flat_workgroup_size: 320
    .name:           _Z7k_headsPKfS0_S0_S0_S0_Pf
    .private_segment_fixed_size: 0
    .sgpr_count:     22
    .sgpr_spill_count: 0
    .symbol:         _Z7k_headsPKfS0_S0_S0_S0_Pf.kd
    .uniform_work_group_size: 1
    .uses_dynamic_stack: false
    .vgpr_count:     56
    .vgpr_spill_count: 0
    .wavefront_size: 64
